# gate|up: leading half starts its SwiGLU epilogue during the trailing half's last MFMA block; its alignment barrier moved behind the 2nd row group
# baseline (speedup 1.0000x reference)
; __device__ __forceinline__ unsigned cvt_pk_bf16(float lo, float hi) { const f32x2_t v = {lo, hi}; const bf16x2_t b = __builtin_convertvector(v, bf16x2_t); return __builtin_bit_cast(unsigned, b); }
; #define PG8_BAR __builtin_amdgcn_s_barrier()
;     __device__ __forceinline__ void operator()(const f32x4 (&acc)[2][2][4][2], const Unit& u, int wr, int wc, int fr, int fq, int ui) const {
;     ...
;         for (int ai = 0; ai < 2; ++ai)
; #pragma unroll
;             for (int m = 0; m < 4; ++m) rs[ai][m] = rtab[ui * 256 + ai * HALF + wr * 64 + m * 16 + fr];
; #pragma unroll
;         for (int ai = 0; ai < 2; ++ai)
; #pragma unroll
;             for (int m = 0; m < 4; ++m) {
;                 const float r = rs[ai][m]; const int row = u.pm * BM + ai * HALF + wr * 64 + m * 16 + fr;
;                 float g[8], v[8], e[8];
; #pragma unroll
;                 for (int n = 0; n < 2; ++n)
; #pragma unroll
;                     for (int i = 0; i < 4; ++i) { g[n * 4 + i] = fmaf(acc[ai][0][m][n][i], r, bg[n][i]); v[n * 4 + i] = fmaf(acc[ai][1][m][n][i], r, bu[n][i]); }
; #pragma unroll
;                 for (int i = 0; i < 8; ++i) e[i] = __builtin_amdgcn_exp2f(g[i] * (-LOG2E));
; #pragma unroll
;                 for (int i = 0; i < 8; ++i) e[i] = __builtin_amdgcn_rcpf(1.0f + e[i]);
; #pragma unroll
;                 for (int i = 0; i < 8; ++i) e[i] = (g[i] * e[i]) * v[i];
;                 u32x4 w; w.x = cvt_pk_bf16(e[0], e[1]); w.y = cvt_pk_bf16(e[2], e[3]); w.z = cvt_pk_bf16(e[4], e[5]); w.w = cvt_pk_bf16(e[6], e[7]);
;                 *(u32x4*)(act + ((size_t)((row >> 8) * (F / 64) + (jcol >> 6)) * 256 + (row & 255)) * 64 + (jcol & 63)) = w;
; template <class Epi, class Sched, bool ALIGN_EPI>
; __device__ __forceinline__ void gemm_phase(PG8_LAS unsigned char* lds, const Gemm g, const Sched& S, const Epi& E, const int tid) {
;     ...
;         }
;         if constexpr (ALIGN_EPI) { if (wr == 0) PG8_BAR; }
;         E(acc, cur, wr, wc, fr, fq, ui); S.done(cur);
.LBB0_249:
	v_lshl_add_u32 v162, s56, 8, v171
	v_lshl_add_u32 v162, v162, 2, 0
	v_lshl_add_u32 v84, s56, 10, v179
	v_add_u32_e32 v162, 0x22000, v162
	ds_read_b128 v[96:99], v84
	ds_read_b128 v[80:83], v84 offset:16
	ds_read_b128 v[100:103], v84 offset:512
	ds_read_b128 v[84:87], v84 offset:528
	ds_read2_b32 v[166:167], v162 offset1:16
	ds_read2_b32 v[176:177], v162 offset0:32 offset1:48
	ds_read2_b32 v[164:165], v162 offset0:128 offset1:144
	ds_read2_b32 v[162:163], v162 offset0:160 offset1:176
	s_lshl_b32 s11, s55, 8
	s_waitcnt lgkmcnt(0)
	v_mov_b32_e32 v222, 0xbfb8aa3b
	v_mov_b32_e32 v224, 1.0
	s_lshl_b32 s9, s57, 7
	s_add_i32 s16, s11, s49
	s_or_b32 s9, s9, s50
	s_ashr_i32 s16, s16, 8
	s_ashr_i32 s9, s9, 6
	s_mulk_i32 s16, 0x58
	s_add_i32 s16, s16, s9
	s_ashr_i32 s17, s16, 31
	s_lshl_b64 s[16:17], s[16:17], 15
	s_add_u32 s16, s16, 0x1000
	s_addc_u32 s17, s17, 0
	v_lshl_add_u64 v[214:215], v[154:155], 0, s[16:17]
	v_lshl_add_u64 v[214:215], v[214:215], 0, v[128:129]
	s_add_i32 s11, s11, s53
	s_ashr_i32 s11, s11, 8
	s_mulk_i32 s11, 0x58
	s_add_i32 s16, s11, s9
	s_ashr_i32 s17, s16, 31
	s_lshl_b64 s[16:17], s[16:17], 15
	s_add_u32 s16, s16, 0x1000
	s_addc_u32 s17, s17, 0
	v_lshl_add_u64 v[216:217], v[156:157], 0, s[16:17]
	v_lshl_add_u64 v[216:217], v[216:217], 0, v[128:129]
	s_mov_b64 s[16:17], -1
	s_movk_i32 s18, 0x1000
	s_mov_b32 s65, s67
	v_pk_fma_f32 v[142:143], v[142:143], v[166:167], v[96:97] op_sel_hi:[1,0,1]
	v_pk_fma_f32 v[144:145], v[144:145], v[166:167], v[98:99] op_sel_hi:[1,0,1]
	v_pk_fma_f32 v[134:135], v[134:135], v[166:167], v[80:81] op_sel_hi:[1,0,1]
	v_pk_fma_f32 v[136:137], v[136:137], v[166:167], v[82:83] op_sel_hi:[1,0,1]
	v_pk_mul_f32 v[198:199], v[142:143], v[222:223] op_sel_hi:[1,0]
	v_pk_mul_f32 v[200:201], v[144:145], v[222:223] op_sel_hi:[1,0]
	v_pk_mul_f32 v[202:203], v[134:135], v[222:223] op_sel_hi:[1,0]
	v_pk_mul_f32 v[204:205], v[136:137], v[222:223] op_sel_hi:[1,0]
	v_pk_fma_f32 v[138:139], v[138:139], v[166:167], v[100:101] op_sel_hi:[1,0,1]
	v_pk_fma_f32 v[140:141], v[140:141], v[166:167], v[102:103] op_sel_hi:[1,0,1]
	v_pk_fma_f32 v[130:131], v[130:131], v[166:167], v[84:85] op_sel_hi:[1,0,1]
	v_pk_fma_f32 v[132:133], v[132:133], v[166:167], v[86:87] op_sel_hi:[1,0,1]
	v_exp_f32_e32 v198, v198
	v_exp_f32_e32 v199, v199
	v_exp_f32_e32 v200, v200
	v_exp_f32_e32 v201, v201
	v_exp_f32_e32 v202, v202
	v_exp_f32_e32 v203, v203
	v_exp_f32_e32 v204, v204
	v_exp_f32_e32 v205, v205
	v_pk_add_f32 v[198:199], v[198:199], v[224:225] op_sel_hi:[1,0]
	v_pk_add_f32 v[200:201], v[200:201], v[224:225] op_sel_hi:[1,0]
	v_pk_add_f32 v[202:203], v[202:203], v[224:225] op_sel_hi:[1,0]
	v_pk_add_f32 v[204:205], v[204:205], v[224:225] op_sel_hi:[1,0]
	v_rcp_f32_e32 v198, v198
	v_rcp_f32_e32 v199, v199
	v_rcp_f32_e32 v200, v200
	v_rcp_f32_e32 v201, v201
	v_rcp_f32_e32 v202, v202
	v_rcp_f32_e32 v203, v203
	v_rcp_f32_e32 v204, v204
	v_rcp_f32_e32 v205, v205
	v_pk_mul_f32 v[142:143], v[142:143], v[198:199]
	v_pk_mul_f32 v[144:145], v[144:145], v[200:201]
	v_pk_mul_f32 v[134:135], v[134:135], v[202:203]
	v_pk_mul_f32 v[136:137], v[136:137], v[204:205]
	v_pk_mul_f32 v[142:143], v[138:139], v[142:143]
	v_pk_mul_f32 v[144:145], v[140:141], v[144:145]
	v_pk_mul_f32 v[134:135], v[130:131], v[134:135]
	v_pk_mul_f32 v[136:137], v[132:133], v[136:137]
	v_cvt_pk_bf16_f32 v206, v142, v143
	v_cvt_pk_bf16_f32 v207, v144, v145
	v_cvt_pk_bf16_f32 v208, v134, v135
	v_cvt_pk_bf16_f32 v209, v136, v137
	global_store_dwordx4 v[214:215], v[206:209], off offset:-4096
	v_pk_fma_f32 v[124:125], v[124:125], v[166:167], v[96:97] op_sel:[0,1,0]
	v_pk_fma_f32 v[126:127], v[126:127], v[166:167], v[98:99] op_sel:[0,1,0]
	v_pk_fma_f32 v[116:117], v[116:117], v[166:167], v[80:81] op_sel:[0,1,0]
	v_pk_fma_f32 v[118:119], v[118:119], v[166:167], v[82:83] op_sel:[0,1,0]
	v_pk_mul_f32 v[198:199], v[124:125], v[222:223] op_sel_hi:[1,0]
	v_pk_mul_f32 v[200:201], v[126:127], v[222:223] op_sel_hi:[1,0]
	v_pk_mul_f32 v[202:203], v[116:117], v[222:223] op_sel_hi:[1,0]
	v_pk_mul_f32 v[204:205], v[118:119], v[222:223] op_sel_hi:[1,0]
	v_pk_fma_f32 v[120:121], v[120:121], v[166:167], v[100:101] op_sel:[0,1,0]
	v_pk_fma_f32 v[122:123], v[122:123], v[166:167], v[102:103] op_sel:[0,1,0]
	v_pk_fma_f32 v[112:113], v[112:113], v[166:167], v[84:85] op_sel:[0,1,0]
	v_pk_fma_f32 v[114:115], v[114:115], v[166:167], v[86:87] op_sel:[0,1,0]
	v_exp_f32_e32 v198, v198
	v_exp_f32_e32 v199, v199
	v_exp_f32_e32 v200, v200
	v_exp_f32_e32 v201, v201
	v_exp_f32_e32 v202, v202
	v_exp_f32_e32 v203, v203
	v_exp_f32_e32 v204, v204
	v_exp_f32_e32 v205, v205
	v_pk_add_f32 v[198:199], v[198:199], v[224:225] op_sel_hi:[1,0]
	v_pk_add_f32 v[200:201], v[200:201], v[224:225] op_sel_hi:[1,0]
	v_pk_add_f32 v[202:203], v[202:203], v[224:225] op_sel_hi:[1,0]
	v_pk_add_f32 v[204:205], v[204:205], v[224:225] op_sel_hi:[1,0]
	v_rcp_f32_e32 v198, v198
	v_rcp_f32_e32 v199, v199
	v_rcp_f32_e32 v200, v200
	v_rcp_f32_e32 v201, v201
	v_rcp_f32_e32 v202, v202
	v_rcp_f32_e32 v203, v203
	v_rcp_f32_e32 v204, v204
	v_rcp_f32_e32 v205, v205
	v_pk_mul_f32 v[124:125], v[124:125], v[198:199]
	v_pk_mul_f32 v[126:127], v[126:127], v[200:201]
	v_pk_mul_f32 v[116:117], v[116:117], v[202:203]
	v_pk_mul_f32 v[118:119], v[118:119], v[204:205]
	v_pk_mul_f32 v[124:125], v[120:121], v[124:125]
	v_pk_mul_f32 v[126:127], v[122:123], v[126:127]
	v_pk_mul_f32 v[116:117], v[112:113], v[116:117]
	v_pk_mul_f32 v[118:119], v[114:115], v[118:119]
	v_cvt_pk_bf16_f32 v210, v124, v125
	v_cvt_pk_bf16_f32 v211, v126, v127
	v_cvt_pk_bf16_f32 v212, v116, v117
	v_cvt_pk_bf16_f32 v213, v118, v119
	global_store_dwordx4 v[214:215], v[210:213], off offset:-2048
	s_and_b64 vcc, exec, s[6:7]
	s_cbranch_vccz .Lgu_bar1
	s_barrier
; __device__ __forceinline__ unsigned cvt_pk_bf16(float lo, float hi) { const f32x2_t v = {lo, hi}; const bf16x2_t b = __builtin_convertvector(v, bf16x2_t); return __builtin_bit_cast(unsigned, b); }
;     __device__ __forceinline__ void operator()(const f32x4 (&acc)[2][2][4][2], const Unit& u, int wr, int wc, int fr, int fq, int ui) const {
;     ...
;                 for (int n = 0; n < 2; ++n)
; #pragma unroll
;                     for (int i = 0; i < 4; ++i) { g[n * 4 + i] = fmaf(acc[ai][0][m][n][i], r, bg[n][i]); v[n * 4 + i] = fmaf(acc[ai][1][m][n][i], r, bu[n][i]); }
; #pragma unroll
;                 for (int i = 0; i < 8; ++i) e[i] = __builtin_amdgcn_exp2f(g[i] * (-LOG2E));
; #pragma unroll
;                 for (int i = 0; i < 8; ++i) e[i] = __builtin_amdgcn_rcpf(1.0f + e[i]);
; #pragma unroll
;                 for (int i = 0; i < 8; ++i) e[i] = (g[i] * e[i]) * v[i];
;                 u32x4 w; w.x = cvt_pk_bf16(e[0], e[1]); w.y = cvt_pk_bf16(e[2], e[3]); w.z = cvt_pk_bf16(e[4], e[5]); w.w = cvt_pk_bf16(e[6], e[7]);
;                 *(u32x4*)(act + ((size_t)((row >> 8) * (F / 64) + (jcol >> 6)) * 256 + (row & 255)) * 64 + (jcol & 63)) = w;
.Lgu_bar1:
	v_pk_fma_f32 v[108:109], v[108:109], v[176:177], v[96:97] op_sel_hi:[1,0,1]
	v_pk_fma_f32 v[110:111], v[110:111], v[176:177], v[98:99] op_sel_hi:[1,0,1]
	v_pk_fma_f32 v[92:93], v[92:93], v[176:177], v[80:81] op_sel_hi:[1,0,1]
	v_pk_fma_f32 v[94:95], v[94:95], v[176:177], v[82:83] op_sel_hi:[1,0,1]
	v_pk_mul_f32 v[198:199], v[108:109], v[222:223] op_sel_hi:[1,0]
	v_pk_mul_f32 v[200:201], v[110:111], v[222:223] op_sel_hi:[1,0]
	v_pk_mul_f32 v[202:203], v[92:93], v[222:223] op_sel_hi:[1,0]
	v_pk_mul_f32 v[204:205], v[94:95], v[222:223] op_sel_hi:[1,0]
	v_pk_fma_f32 v[104:105], v[104:105], v[176:177], v[100:101] op_sel_hi:[1,0,1]
	v_pk_fma_f32 v[106:107], v[106:107], v[176:177], v[102:103] op_sel_hi:[1,0,1]
	v_pk_fma_f32 v[88:89], v[88:89], v[176:177], v[84:85] op_sel_hi:[1,0,1]
	v_pk_fma_f32 v[90:91], v[90:91], v[176:177], v[86:87] op_sel_hi:[1,0,1]
	v_exp_f32_e32 v198, v198
	v_exp_f32_e32 v199, v199
	v_exp_f32_e32 v200, v200
	v_exp_f32_e32 v201, v201
	v_exp_f32_e32 v202, v202
	v_exp_f32_e32 v203, v203
	v_exp_f32_e32 v204, v204
	v_exp_f32_e32 v205, v205
	v_pk_add_f32 v[198:199], v[198:199], v[224:225] op_sel_hi:[1,0]
	v_pk_add_f32 v[200:201], v[200:201], v[224:225] op_sel_hi:[1,0]
	v_pk_add_f32 v[202:203], v[202:203], v[224:225] op_sel_hi:[1,0]
	v_pk_add_f32 v[204:205], v[204:205], v[224:225] op_sel_hi:[1,0]
	v_rcp_f32_e32 v198, v198
	v_rcp_f32_e32 v199, v199
	v_rcp_f32_e32 v200, v200
	v_rcp_f32_e32 v201, v201
	v_rcp_f32_e32 v202, v202
	v_rcp_f32_e32 v203, v203
	v_rcp_f32_e32 v204, v204
	v_rcp_f32_e32 v205, v205
	v_pk_mul_f32 v[108:109], v[108:109], v[198:199]
	v_pk_mul_f32 v[110:111], v[110:111], v[200:201]
	v_pk_mul_f32 v[92:93], v[92:93], v[202:203]
	v_pk_mul_f32 v[94:95], v[94:95], v[204:205]
	v_pk_mul_f32 v[108:109], v[104:105], v[108:109]
	v_pk_mul_f32 v[110:111], v[106:107], v[110:111]
	v_pk_mul_f32 v[92:93], v[88:89], v[92:93]
	v_pk_mul_f32 v[94:95], v[90:91], v[94:95]
	v_cvt_pk_bf16_f32 v206, v108, v109
	v_cvt_pk_bf16_f32 v207, v110, v111
	v_cvt_pk_bf16_f32 v208, v92, v93
	v_cvt_pk_bf16_f32 v209, v94, v95
	global_store_dwordx4 v[214:215], v[206:209], off
	v_pk_fma_f32 v[76:77], v[76:77], v[176:177], v[96:97] op_sel:[0,1,0]
	v_pk_fma_f32 v[78:79], v[78:79], v[176:177], v[98:99] op_sel:[0,1,0]
	v_pk_fma_f32 v[68:69], v[68:69], v[176:177], v[80:81] op_sel:[0,1,0]
	v_pk_fma_f32 v[70:71], v[70:71], v[176:177], v[82:83] op_sel:[0,1,0]
	v_pk_mul_f32 v[198:199], v[76:77], v[222:223] op_sel_hi:[1,0]
	v_pk_mul_f32 v[200:201], v[78:79], v[222:223] op_sel_hi:[1,0]
	v_pk_mul_f32 v[202:203], v[68:69], v[222:223] op_sel_hi:[1,0]
	v_pk_mul_f32 v[204:205], v[70:71], v[222:223] op_sel_hi:[1,0]
	v_pk_fma_f32 v[72:73], v[72:73], v[176:177], v[100:101] op_sel:[0,1,0]
	v_pk_fma_f32 v[74:75], v[74:75], v[176:177], v[102:103] op_sel:[0,1,0]
	v_pk_fma_f32 v[64:65], v[64:65], v[176:177], v[84:85] op_sel:[0,1,0]
	v_pk_fma_f32 v[66:67], v[66:67], v[176:177], v[86:87] op_sel:[0,1,0]
	v_exp_f32_e32 v198, v198
	v_exp_f32_e32 v199, v199
	v_exp_f32_e32 v200, v200
	v_exp_f32_e32 v201, v201
	v_exp_f32_e32 v202, v202
	v_exp_f32_e32 v203, v203
	v_exp_f32_e32 v204, v204
	v_exp_f32_e32 v205, v205
	v_pk_add_f32 v[198:199], v[198:199], v[224:225] op_sel_hi:[1,0]
	v_pk_add_f32 v[200:201], v[200:201], v[224:225] op_sel_hi:[1,0]
	v_pk_add_f32 v[202:203], v[202:203], v[224:225] op_sel_hi:[1,0]
	v_pk_add_f32 v[204:205], v[204:205], v[224:225] op_sel_hi:[1,0]
	v_rcp_f32_e32 v198, v198
	v_rcp_f32_e32 v199, v199
	v_rcp_f32_e32 v200, v200
	v_rcp_f32_e32 v201, v201
	v_rcp_f32_e32 v202, v202
	v_rcp_f32_e32 v203, v203
	v_rcp_f32_e32 v204, v204
	v_rcp_f32_e32 v205, v205
	v_pk_mul_f32 v[76:77], v[76:77], v[198:199]
	v_pk_mul_f32 v[78:79], v[78:79], v[200:201]
	v_pk_mul_f32 v[68:69], v[68:69], v[202:203]
	v_pk_mul_f32 v[70:71], v[70:71], v[204:205]
	v_pk_mul_f32 v[76:77], v[72:73], v[76:77]
	v_pk_mul_f32 v[78:79], v[74:75], v[78:79]
	v_pk_mul_f32 v[68:69], v[64:65], v[68:69]
	v_pk_mul_f32 v[70:71], v[66:67], v[70:71]
	v_cvt_pk_bf16_f32 v210, v76, v77
	v_cvt_pk_bf16_f32 v211, v78, v79
	v_cvt_pk_bf16_f32 v212, v68, v69
	v_cvt_pk_bf16_f32 v213, v70, v71
	global_store_dwordx4 v[214:215], v[210:213], off offset:2048
	v_pk_fma_f32 v[60:61], v[60:61], v[164:165], v[96:97] op_sel_hi:[1,0,1]
	v_pk_fma_f32 v[62:63], v[62:63], v[164:165], v[98:99] op_sel_hi:[1,0,1]
	v_pk_fma_f32 v[52:53], v[52:53], v[164:165], v[80:81] op_sel_hi:[1,0,1]
	v_pk_fma_f32 v[54:55], v[54:55], v[164:165], v[82:83] op_sel_hi:[1,0,1]
	v_pk_mul_f32 v[198:199], v[60:61], v[222:223] op_sel_hi:[1,0]
	v_pk_mul_f32 v[200:201], v[62:63], v[222:223] op_sel_hi:[1,0]
	v_pk_mul_f32 v[202:203], v[52:53], v[222:223] op_sel_hi:[1,0]
	v_pk_mul_f32 v[204:205], v[54:55], v[222:223] op_sel_hi:[1,0]
	v_pk_fma_f32 v[56:57], v[56:57], v[164:165], v[100:101] op_sel_hi:[1,0,1]
	v_pk_fma_f32 v[58:59], v[58:59], v[164:165], v[102:103] op_sel_hi:[1,0,1]
	v_pk_fma_f32 v[48:49], v[48:49], v[164:165], v[84:85] op_sel_hi:[1,0,1]
	v_pk_fma_f32 v[50:51], v[50:51], v[164:165], v[86:87] op_sel_hi:[1,0,1]
	v_exp_f32_e32 v198, v198
	v_exp_f32_e32 v199, v199
	v_exp_f32_e32 v200, v200
	v_exp_f32_e32 v201, v201
	v_exp_f32_e32 v202, v202
	v_exp_f32_e32 v203, v203
	v_exp_f32_e32 v204, v204
	v_exp_f32_e32 v205, v205
	v_pk_add_f32 v[198:199], v[198:199], v[224:225] op_sel_hi:[1,0]
	v_pk_add_f32 v[200:201], v[200:201], v[224:225] op_sel_hi:[1,0]
	v_pk_add_f32 v[202:203], v[202:203], v[224:225] op_sel_hi:[1,0]
	v_pk_add_f32 v[204:205], v[204:205], v[224:225] op_sel_hi:[1,0]
	v_rcp_f32_e32 v198, v198
	v_rcp_f32_e32 v199, v199
	v_rcp_f32_e32 v200, v200
	v_rcp_f32_e32 v201, v201
	v_rcp_f32_e32 v202, v202
	v_rcp_f32_e32 v203, v203
	v_rcp_f32_e32 v204, v204
; __device__ __forceinline__ unsigned cvt_pk_bf16(float lo, float hi) { const f32x2_t v = {lo, hi}; const bf16x2_t b = __builtin_convertvector(v, bf16x2_t); return __builtin_bit_cast(unsigned, b); }
; #define PG8_BAR __builtin_amdgcn_s_barrier()
;     __device__ __forceinline__ void operator()(const f32x4 (&acc)[2][2][4][2], const Unit& u, int wr, int wc, int fr, int fq, int ui) const {
;     ...
;                 for (int n = 0; n < 2; ++n)
; #pragma unroll
;                     for (int i = 0; i < 4; ++i) { g[n * 4 + i] = fmaf(acc[ai][0][m][n][i], r, bg[n][i]); v[n * 4 + i] = fmaf(acc[ai][1][m][n][i], r, bu[n][i]); }
; #pragma unroll
;                 for (int i = 0; i < 8; ++i) e[i] = __builtin_amdgcn_exp2f(g[i] * (-LOG2E));
; #pragma unroll
;                 for (int i = 0; i < 8; ++i) e[i] = __builtin_amdgcn_rcpf(1.0f + e[i]);
; #pragma unroll
;                 for (int i = 0; i < 8; ++i) e[i] = (g[i] * e[i]) * v[i];
;                 u32x4 w; w.x = cvt_pk_bf16(e[0], e[1]); w.y = cvt_pk_bf16(e[2], e[3]); w.z = cvt_pk_bf16(e[4], e[5]); w.w = cvt_pk_bf16(e[6], e[7]);
;                 *(u32x4*)(act + ((size_t)((row >> 8) * (F / 64) + (jcol >> 6)) * 256 + (row & 255)) * 64 + (jcol & 63)) = w;
; template <class Epi, class Sched, bool ALIGN_EPI>
; __device__ __forceinline__ void gemm_phase(PG8_LAS unsigned char* lds, const Gemm g, const Sched& S, const Epi& E, const int tid) {
;     ...
;         }
;         if constexpr (ALIGN_EPI) { if (wr == 0) PG8_BAR; }
;         E(acc, cur, wr, wc, fr, fq, ui); S.done(cur);
;         if (!has_next) break;
; #pragma unroll
;         for (int a = 0; a < 2; ++a)
; #pragma unroll
;             for (int b = 0; b < 2; ++b)
; #pragma unroll
;                 for (int m = 0; m < 4; ++m)
; #pragma unroll
;                     for (int n = 0; n < 2; ++n) acc[a][b][m][n] = (f32x4){0.f, 0.f, 0.f, 0.f};
;         cur = nxt; cA = nA; cB = nB; ++ui;
;         if constexpr (ALIGN_EPI) { if (wr == 1) PG8_BAR; }
	v_rcp_f32_e32 v205, v205
	v_pk_mul_f32 v[60:61], v[60:61], v[198:199]
	v_pk_mul_f32 v[62:63], v[62:63], v[200:201]
	v_pk_mul_f32 v[52:53], v[52:53], v[202:203]
	v_pk_mul_f32 v[54:55], v[54:55], v[204:205]
	v_pk_mul_f32 v[60:61], v[56:57], v[60:61]
	v_pk_mul_f32 v[62:63], v[58:59], v[62:63]
	v_pk_mul_f32 v[52:53], v[48:49], v[52:53]
	v_pk_mul_f32 v[54:55], v[50:51], v[54:55]
	v_cvt_pk_bf16_f32 v206, v60, v61
	v_cvt_pk_bf16_f32 v207, v62, v63
	v_cvt_pk_bf16_f32 v208, v52, v53
	v_cvt_pk_bf16_f32 v209, v54, v55
	global_store_dwordx4 v[216:217], v[206:209], off offset:-4096
	v_pk_fma_f32 v[44:45], v[44:45], v[164:165], v[96:97] op_sel:[0,1,0]
	v_pk_fma_f32 v[46:47], v[46:47], v[164:165], v[98:99] op_sel:[0,1,0]
	v_pk_fma_f32 v[36:37], v[36:37], v[164:165], v[80:81] op_sel:[0,1,0]
	v_pk_fma_f32 v[38:39], v[38:39], v[164:165], v[82:83] op_sel:[0,1,0]
	v_pk_mul_f32 v[198:199], v[44:45], v[222:223] op_sel_hi:[1,0]
	v_pk_mul_f32 v[200:201], v[46:47], v[222:223] op_sel_hi:[1,0]
	v_pk_mul_f32 v[202:203], v[36:37], v[222:223] op_sel_hi:[1,0]
	v_pk_mul_f32 v[204:205], v[38:39], v[222:223] op_sel_hi:[1,0]
	v_pk_fma_f32 v[40:41], v[40:41], v[164:165], v[100:101] op_sel:[0,1,0]
	v_pk_fma_f32 v[42:43], v[42:43], v[164:165], v[102:103] op_sel:[0,1,0]
	v_pk_fma_f32 v[32:33], v[32:33], v[164:165], v[84:85] op_sel:[0,1,0]
	v_pk_fma_f32 v[34:35], v[34:35], v[164:165], v[86:87] op_sel:[0,1,0]
	v_exp_f32_e32 v198, v198
	v_exp_f32_e32 v199, v199
	v_exp_f32_e32 v200, v200
	v_exp_f32_e32 v201, v201
	v_exp_f32_e32 v202, v202
	v_exp_f32_e32 v203, v203
	v_exp_f32_e32 v204, v204
	v_exp_f32_e32 v205, v205
	v_pk_add_f32 v[198:199], v[198:199], v[224:225] op_sel_hi:[1,0]
	v_pk_add_f32 v[200:201], v[200:201], v[224:225] op_sel_hi:[1,0]
	v_pk_add_f32 v[202:203], v[202:203], v[224:225] op_sel_hi:[1,0]
	v_pk_add_f32 v[204:205], v[204:205], v[224:225] op_sel_hi:[1,0]
	v_rcp_f32_e32 v198, v198
	v_rcp_f32_e32 v199, v199
	v_rcp_f32_e32 v200, v200
	v_rcp_f32_e32 v201, v201
	v_rcp_f32_e32 v202, v202
	v_rcp_f32_e32 v203, v203
	v_rcp_f32_e32 v204, v204
	v_rcp_f32_e32 v205, v205
	v_pk_mul_f32 v[44:45], v[44:45], v[198:199]
	v_pk_mul_f32 v[46:47], v[46:47], v[200:201]
	v_pk_mul_f32 v[36:37], v[36:37], v[202:203]
	v_pk_mul_f32 v[38:39], v[38:39], v[204:205]
	v_pk_mul_f32 v[44:45], v[40:41], v[44:45]
	v_pk_mul_f32 v[46:47], v[42:43], v[46:47]
	v_pk_mul_f32 v[36:37], v[32:33], v[36:37]
	v_pk_mul_f32 v[38:39], v[34:35], v[38:39]
	v_cvt_pk_bf16_f32 v210, v44, v45
	v_cvt_pk_bf16_f32 v211, v46, v47
	v_cvt_pk_bf16_f32 v212, v36, v37
	v_cvt_pk_bf16_f32 v213, v38, v39
	global_store_dwordx4 v[216:217], v[210:213], off offset:-2048
	v_pk_fma_f32 v[28:29], v[28:29], v[162:163], v[96:97] op_sel_hi:[1,0,1]
	v_pk_fma_f32 v[30:31], v[30:31], v[162:163], v[98:99] op_sel_hi:[1,0,1]
	v_pk_fma_f32 v[20:21], v[20:21], v[162:163], v[80:81] op_sel_hi:[1,0,1]
	v_pk_fma_f32 v[22:23], v[22:23], v[162:163], v[82:83] op_sel_hi:[1,0,1]
	v_pk_mul_f32 v[198:199], v[28:29], v[222:223] op_sel_hi:[1,0]
	v_pk_mul_f32 v[200:201], v[30:31], v[222:223] op_sel_hi:[1,0]
	v_pk_mul_f32 v[202:203], v[20:21], v[222:223] op_sel_hi:[1,0]
	v_pk_mul_f32 v[204:205], v[22:23], v[222:223] op_sel_hi:[1,0]
	v_pk_fma_f32 v[24:25], v[24:25], v[162:163], v[100:101] op_sel_hi:[1,0,1]
	v_pk_fma_f32 v[26:27], v[26:27], v[162:163], v[102:103] op_sel_hi:[1,0,1]
	v_pk_fma_f32 v[16:17], v[16:17], v[162:163], v[84:85] op_sel_hi:[1,0,1]
	v_pk_fma_f32 v[18:19], v[18:19], v[162:163], v[86:87] op_sel_hi:[1,0,1]
	v_exp_f32_e32 v198, v198
	v_exp_f32_e32 v199, v199
	v_exp_f32_e32 v200, v200
	v_exp_f32_e32 v201, v201
	v_exp_f32_e32 v202, v202
	v_exp_f32_e32 v203, v203
	v_exp_f32_e32 v204, v204
	v_exp_f32_e32 v205, v205
	v_pk_add_f32 v[198:199], v[198:199], v[224:225] op_sel_hi:[1,0]
	v_pk_add_f32 v[200:201], v[200:201], v[224:225] op_sel_hi:[1,0]
	v_pk_add_f32 v[202:203], v[202:203], v[224:225] op_sel_hi:[1,0]
	v_pk_add_f32 v[204:205], v[204:205], v[224:225] op_sel_hi:[1,0]
	v_rcp_f32_e32 v198, v198
	v_rcp_f32_e32 v199, v199
	v_rcp_f32_e32 v200, v200
	v_rcp_f32_e32 v201, v201
	v_rcp_f32_e32 v202, v202
	v_rcp_f32_e32 v203, v203
	v_rcp_f32_e32 v204, v204
	v_rcp_f32_e32 v205, v205
	v_pk_mul_f32 v[28:29], v[28:29], v[198:199]
	v_pk_mul_f32 v[30:31], v[30:31], v[200:201]
	v_pk_mul_f32 v[20:21], v[20:21], v[202:203]
	v_pk_mul_f32 v[22:23], v[22:23], v[204:205]
	v_pk_mul_f32 v[28:29], v[24:25], v[28:29]
	v_pk_mul_f32 v[30:31], v[26:27], v[30:31]
	v_pk_mul_f32 v[20:21], v[16:17], v[20:21]
	v_pk_mul_f32 v[22:23], v[18:19], v[22:23]
	v_cvt_pk_bf16_f32 v206, v28, v29
	v_cvt_pk_bf16_f32 v207, v30, v31
	v_cvt_pk_bf16_f32 v208, v20, v21
	v_cvt_pk_bf16_f32 v209, v22, v23
	global_store_dwordx4 v[216:217], v[206:209], off
	v_pk_fma_f32 v[12:13], v[12:13], v[162:163], v[96:97] op_sel:[0,1,0]
	v_pk_fma_f32 v[14:15], v[14:15], v[162:163], v[98:99] op_sel:[0,1,0]
	v_pk_fma_f32 v[4:5], v[4:5], v[162:163], v[80:81] op_sel:[0,1,0]
	v_pk_fma_f32 v[6:7], v[6:7], v[162:163], v[82:83] op_sel:[0,1,0]
	v_pk_mul_f32 v[198:199], v[12:13], v[222:223] op_sel_hi:[1,0]
	v_pk_mul_f32 v[200:201], v[14:15], v[222:223] op_sel_hi:[1,0]
	v_pk_mul_f32 v[202:203], v[4:5], v[222:223] op_sel_hi:[1,0]
	v_pk_mul_f32 v[204:205], v[6:7], v[222:223] op_sel_hi:[1,0]
	v_pk_fma_f32 v[8:9], v[8:9], v[162:163], v[100:101] op_sel:[0,1,0]
	v_pk_fma_f32 v[10:11], v[10:11], v[162:163], v[102:103] op_sel:[0,1,0]
	v_pk_fma_f32 v[0:1], v[0:1], v[162:163], v[84:85] op_sel:[0,1,0]
	v_pk_fma_f32 v[2:3], v[2:3], v[162:163], v[86:87] op_sel:[0,1,0]
	v_exp_f32_e32 v198, v198
	v_exp_f32_e32 v199, v199
	v_exp_f32_e32 v200, v200
	v_exp_f32_e32 v201, v201
	v_exp_f32_e32 v202, v202
	v_exp_f32_e32 v203, v203
	v_exp_f32_e32 v204, v204
	v_exp_f32_e32 v205, v205
	v_pk_add_f32 v[198:199], v[198:199], v[224:225] op_sel_hi:[1,0]
	v_pk_add_f32 v[200:201], v[200:201], v[224:225] op_sel_hi:[1,0]
	v_pk_add_f32 v[202:203], v[202:203], v[224:225] op_sel_hi:[1,0]
	v_pk_add_f32 v[204:205], v[204:205], v[224:225] op_sel_hi:[1,0]
	v_rcp_f32_e32 v198, v198
	v_rcp_f32_e32 v199, v199
	v_rcp_f32_e32 v200, v200
	v_rcp_f32_e32 v201, v201
	v_rcp_f32_e32 v202, v202
	v_rcp_f32_e32 v203, v203
	v_rcp_f32_e32 v204, v204
	v_rcp_f32_e32 v205, v205
	v_pk_mul_f32 v[12:13], v[12:13], v[198:199]
	v_pk_mul_f32 v[14:15], v[14:15], v[200:201]
	v_pk_mul_f32 v[4:5], v[4:5], v[202:203]
	v_pk_mul_f32 v[6:7], v[6:7], v[204:205]
	v_pk_mul_f32 v[12:13], v[8:9], v[12:13]
	v_pk_mul_f32 v[14:15], v[10:11], v[14:15]
	v_pk_mul_f32 v[4:5], v[0:1], v[4:5]
	v_pk_mul_f32 v[6:7], v[2:3], v[6:7]
	v_cvt_pk_bf16_f32 v210, v12, v13
	v_cvt_pk_bf16_f32 v211, v14, v15
	v_cvt_pk_bf16_f32 v212, v4, v5
	v_cvt_pk_bf16_f32 v213, v6, v7
	global_store_dwordx4 v[216:217], v[210:213], off offset:2048
	s_andn2_b64 vcc, exec, s[2:3]
	s_cbranch_vccnz .LBB0_242
	s_andn2_b64 vcc, exec, s[4:5]
	s_cbranch_vccnz .LBB0_241
	s_barrier
	s_branch .LBB0_241
